# speedup vs baseline: 1.0056x; 1.0056x over previous
_Z9l1_kernelPKiS0_P15HIP_vector_typeIjLj2EEPiS4_PKfS6_S6_S6_PfP6__half:
	s_cmp_gt_u32 s2, 42
	s_mov_b64 s[4:5], -1
	s_cbranch_scc0 .LBB0_17
	s_mul_i32 s15, s2, 0xeb
	s_add_i32 s3, s15, 0xffffd887
	s_min_i32 s16, s3, 0xc265
	s_add_i32 s12, s16, 0xeb
	s_cmp_ge_i32 s3, s12
	s_cbranch_scc1 .LBB0_16
	s_load_dwordx4 s[4:7], s[0:1], 0x28
	s_load_dwordx2 s[10:11], s[0:1], 0x38
	s_load_dwordx4 s[24:27], s[0:1], 0x40
	s_load_dwordx2 s[28:29], s[0:1], 0x50
	v_lshlrev_b32_e32 v1, 4, v0
	v_and_b32_e32 v2, 0x1f0, v1
	v_mov_b32_e32 v3, 0
	v_lshrrev_b32_e32 v1, 5, v0
	s_add_i32 s13, s16, 0xea
	s_waitcnt lgkmcnt(0)
	v_lshl_add_u64 v[110:111], s[4:5], 0, v[2:3]
	v_add_u32_e32 v2, s3, v1
	v_min_i32_e32 v2, s13, v2
	v_ashrrev_i32_e32 v3, 31, v2
	v_lshlrev_b64 v[2:3], 9, v[2:3]
	v_lshl_add_u64 v[10:11], v[110:111], 0, v[2:3]
	v_or_b32_e32 v2, 0x200, v0
	v_lshrrev_b32_e32 v146, 5, v2
	v_add_u32_e32 v2, s3, v146
	v_min_i32_e32 v2, s13, v2
	v_ashrrev_i32_e32 v3, 31, v2
	v_lshlrev_b64 v[2:3], 9, v[2:3]
	v_or_b32_e32 v147, 32, v1
	v_lshl_add_u64 v[12:13], v[110:111], 0, v[2:3]
	global_load_dwordx4 v[2:5], v[10:11], off
	global_load_dwordx4 v[6:9], v[12:13], off
	v_add_u32_e32 v10, s3, v147
	v_min_i32_e32 v10, s13, v10
	v_ashrrev_i32_e32 v11, 31, v10
	v_lshlrev_b64 v[10:11], 9, v[10:11]
	v_lshl_add_u64 v[10:11], v[110:111], 0, v[10:11]
	global_load_dwordx4 v[10:13], v[10:11], off
	s_barrier
	v_lshrrev_b32_e32 v149, 6, v0
	s_movk_i32 s4, 0x200
	v_and_b32_e32 v150, 15, v0
	v_cmp_gt_u32_e32 vcc, s4, v0
	v_lshlrev_b32_e32 v151, 4, v149
	s_and_saveexec_b64 s[4:5], vcc
	s_xor_b64 s[4:5], exec, s[4:5]
	v_or_b32_e32 v32, v151, v150
	s_or_saveexec_b64 s[4:5], s[4:5]
	v_lshlrev_b32_e32 v14, 1, v150
	v_mov_b64_e32 v[30:31], s[6:7]
	s_xor_b64 exec, exec, s[4:5]
	v_and_b32_e32 v15, 0x60, v151
	v_bfe_u32 v16, v0, 6, 1
	v_or3_b32 v32, v16, v15, v14
	v_mov_b64_e32 v[30:31], s[10:11]
	s_or_b64 exec, exec, s[4:5]
	s_movk_i32 s17, 0x110
	s_mov_b32 s14, 0x7060302
	s_sub_i32 s19, s16, s3
	s_addk_i32 s19, 0x11a
	v_readfirstlane_b32 s30, v149
	v_bfe_u32 v152, v0, 4, 2
	v_lshlrev_b32_e32 v153, 5, v149
	v_and_b32_e32 v153, 0x60, v153
	v_or_b32_e32 v144, v151, v150
	v_lshlrev_b32_e32 v144, 2, v144
	v_lshl_add_u32 v144, v152, 12, v144
	v_lshlrev_b32_e32 v145, 3, v150
	v_lshl_add_u32 v145, v153, 2, v145
	v_lshl_add_u32 v145, v152, 12, v145
	s_waitcnt lgkmcnt(0)
	s_cmp_lt_u32 s30, 4
	s_cselect_b32 s20, s10, s24
	s_cselect_b32 s21, s11, s25
	s_add_u32 s32, s6, 0x4000
	s_addc_u32 s33, s7, 0
	s_add_u32 s34, s6, 0x8000
	s_addc_u32 s35, s7, 0
	s_add_u32 s36, s6, 0xc000
	s_addc_u32 s37, s7, 0
	s_add_u32 s38, s20, 0x4000
	s_addc_u32 s39, s21, 0
	s_add_u32 s40, s20, 0x8000
	s_addc_u32 s41, s21, 0
	s_add_u32 s42, s20, 0xc000
	s_addc_u32 s43, s21, 0
	s_mul_hi_u32 s5, s19, 0xaaaaaaab
	s_addk_i32 s16, 0xfa
	s_lshr_b32 s10, s5, 5
	s_mov_b32 s11, 0
	s_add_i32 s31, s30, s2
	s_and_b32 s31, s31, 7
	s_cmp_eq_u32 s31, 1
	s_cbranch_scc1 .Lw_rot_1
	s_cmp_eq_u32 s31, 2
	s_cbranch_scc1 .Lw_rot_2
	s_cmp_eq_u32 s31, 3
	s_cbranch_scc1 .Lw_rot_3
	s_cmp_eq_u32 s31, 4
	s_cbranch_scc1 .Lw_rot_4
	s_cmp_eq_u32 s31, 5
	s_cbranch_scc1 .Lw_rot_5
	s_cmp_eq_u32 s31, 6
	s_cbranch_scc1 .Lw_rot_6
	s_cmp_eq_u32 s31, 7
	s_cbranch_scc1 .Lw_rot_7
